# attention P.V: the 16 transposed V reads of each key-tile pair issued together into unused registers, MFMAs with counted waits
# speedup vs baseline: 1.0127x; 1.0031x over previous
.LBB0_392:
	v_readlane_b32 s88, v254, 48
	v_readlane_b32 s89, v254, 49
	s_andn2_b64 vcc, exec, s[66:67]
	s_cbranch_vccnz .LBB0_398
	s_and_b64 s[16:17], s[48:49], exec
	s_cselect_b32 s16, s43, s86
	v_add_u32_e32 v10, s16, v157
	v_add_u32_e32 v252, v10, v149
	ds_read_b64_tr_b16 v[188:189], v252 offset:8192
	ds_read_b64_tr_b16 v[190:191], v252 offset:12288
	v_add_u32_e32 v253, v10, v150
	ds_read_b64_tr_b16 v[192:193], v253 offset:8192
	ds_read_b64_tr_b16 v[194:195], v253 offset:12288
	v_add_u32_e32 v252, v10, v151
	ds_read_b64_tr_b16 v[196:197], v252 offset:8192
	ds_read_b64_tr_b16 v[198:199], v252 offset:12288
	v_add_u32_e32 v253, v10, v152
	ds_read_b64_tr_b16 v[200:201], v253 offset:8192
	ds_read_b64_tr_b16 v[202:203], v253 offset:12288
	v_add_u32_e32 v252, v10, v153
	ds_read_b64_tr_b16 v[204:205], v252 offset:8192
	ds_read_b64_tr_b16 v[206:207], v252 offset:12288
	v_add_u32_e32 v253, v10, v154
	ds_read_b64_tr_b16 v[208:209], v253 offset:8192
	ds_read_b64_tr_b16 v[210:211], v253 offset:12288
	v_add_u32_e32 v252, v10, v155
	ds_read_b64_tr_b16 v[212:213], v252 offset:8192
	ds_read_b64_tr_b16 v[214:215], v252 offset:12288
	v_add_u32_e32 v253, v10, v156
	ds_read_b64_tr_b16 v[216:217], v253 offset:8192
	ds_read_b64_tr_b16 v[218:219], v253 offset:12288
	v_cvt_pk_bf16_f32 v172, v172, v173
	v_cvt_pk_bf16_f32 v173, v174, v175
	v_cvt_pk_bf16_f32 v174, v176, v177
	v_cvt_pk_bf16_f32 v175, v178, v179
	s_nop 1
	s_waitcnt lgkmcnt(14)
	v_mfma_f32_16x16x32_bf16 v[2:5], v[188:191], v[172:175], v[2:5]
	s_waitcnt lgkmcnt(12)
	v_mfma_f32_16x16x32_bf16 v[6:9], v[192:195], v[172:175], v[6:9]
	s_waitcnt lgkmcnt(10)
	v_mfma_f32_16x16x32_bf16 v[58:61], v[196:199], v[172:175], v[58:61]
	s_waitcnt lgkmcnt(8)
	v_mfma_f32_16x16x32_bf16 v[62:65], v[200:203], v[172:175], v[62:65]
	s_waitcnt lgkmcnt(6)
	v_mfma_f32_16x16x32_bf16 v[66:69], v[204:207], v[172:175], v[66:69]
	s_waitcnt lgkmcnt(4)
	v_mfma_f32_16x16x32_bf16 v[74:77], v[208:211], v[172:175], v[74:77]
	s_waitcnt lgkmcnt(2)
	v_mfma_f32_16x16x32_bf16 v[70:73], v[212:215], v[172:175], v[70:73]
	s_waitcnt lgkmcnt(0)
	v_mfma_f32_16x16x32_bf16 v[54:57], v[216:219], v[172:175], v[54:57]
	s_andn2_b64 vcc, exec, s[64:65]
	s_cbranch_vccz .LBB0_399

.LBB0_395:
	s_and_b64 s[16:17], s[56:57], exec
	s_cselect_b32 s16, s43, s86
	v_add_u32_e32 v10, s16, v157
	v_add_u32_e32 v252, v10, v149
	ds_read_b64_tr_b16 v[188:189], v252 offset:24576
	ds_read_b64_tr_b16 v[190:191], v252 offset:28672
	v_add_u32_e32 v253, v10, v150
	ds_read_b64_tr_b16 v[192:193], v253 offset:24576
	ds_read_b64_tr_b16 v[194:195], v253 offset:28672
	v_add_u32_e32 v252, v10, v151
	ds_read_b64_tr_b16 v[196:197], v252 offset:24576
	ds_read_b64_tr_b16 v[198:199], v252 offset:28672
	v_add_u32_e32 v253, v10, v152
	ds_read_b64_tr_b16 v[200:201], v253 offset:24576
	ds_read_b64_tr_b16 v[202:203], v253 offset:28672
	v_add_u32_e32 v252, v10, v153
	ds_read_b64_tr_b16 v[204:205], v252 offset:24576
	ds_read_b64_tr_b16 v[206:207], v252 offset:28672
	v_add_u32_e32 v253, v10, v154
	ds_read_b64_tr_b16 v[208:209], v253 offset:24576
	ds_read_b64_tr_b16 v[210:211], v253 offset:28672
	v_add_u32_e32 v252, v10, v155
	ds_read_b64_tr_b16 v[212:213], v252 offset:24576
	ds_read_b64_tr_b16 v[214:215], v252 offset:28672
	v_add_u32_e32 v253, v10, v156
	ds_read_b64_tr_b16 v[216:217], v253 offset:24576
	ds_read_b64_tr_b16 v[218:219], v253 offset:28672
	v_cvt_pk_bf16_f32 v90, v88, v90
	v_cvt_pk_bf16_f32 v91, v91, v92
	v_cvt_pk_bf16_f32 v92, v93, v161
	v_cvt_pk_bf16_f32 v93, v162, v163
	s_nop 1
	s_waitcnt lgkmcnt(14)
	v_mfma_f32_16x16x32_bf16 v[2:5], v[188:191], v[90:93], v[2:5]
	s_waitcnt lgkmcnt(12)
	v_mfma_f32_16x16x32_bf16 v[6:9], v[192:195], v[90:93], v[6:9]
	s_waitcnt lgkmcnt(10)
	v_mfma_f32_16x16x32_bf16 v[58:61], v[196:199], v[90:93], v[58:61]
	s_waitcnt lgkmcnt(8)
	v_mfma_f32_16x16x32_bf16 v[62:65], v[200:203], v[90:93], v[62:65]
	s_waitcnt lgkmcnt(6)
	v_mfma_f32_16x16x32_bf16 v[66:69], v[204:207], v[90:93], v[66:69]
	s_waitcnt lgkmcnt(4)
	v_mfma_f32_16x16x32_bf16 v[74:77], v[208:211], v[90:93], v[74:77]
	s_waitcnt lgkmcnt(2)
	v_mfma_f32_16x16x32_bf16 v[70:73], v[212:215], v[90:93], v[70:73]
	s_waitcnt lgkmcnt(0)
	v_mfma_f32_16x16x32_bf16 v[54:57], v[216:219], v[90:93], v[54:57]
.LBB0_396:
	v_add_u32_e32 v10, s86, v157
	v_add_u32_e32 v252, v10, v149
	ds_read_b64_tr_b16 v[188:189], v252 offset:32768
	ds_read_b64_tr_b16 v[190:191], v252 offset:36864
	v_add_u32_e32 v253, v10, v151
	ds_read_b64_tr_b16 v[192:193], v253 offset:32768
	ds_read_b64_tr_b16 v[194:195], v253 offset:36864
	v_add_u32_e32 v252, v10, v150
	ds_read_b64_tr_b16 v[196:197], v252 offset:32768
	ds_read_b64_tr_b16 v[198:199], v252 offset:36864
	v_add_u32_e32 v253, v10, v153
	ds_read_b64_tr_b16 v[200:201], v253 offset:32768
	ds_read_b64_tr_b16 v[202:203], v253 offset:36864
	v_add_u32_e32 v252, v10, v152
	ds_read_b64_tr_b16 v[204:205], v252 offset:32768
	ds_read_b64_tr_b16 v[206:207], v252 offset:36864
	v_add_u32_e32 v253, v10, v155
	ds_read_b64_tr_b16 v[208:209], v253 offset:32768
	ds_read_b64_tr_b16 v[210:211], v253 offset:36864
	v_add_u32_e32 v252, v10, v154
	ds_read_b64_tr_b16 v[212:213], v252 offset:32768
	ds_read_b64_tr_b16 v[214:215], v252 offset:36864
	v_add_u32_e32 v253, v10, v156
	ds_read_b64_tr_b16 v[216:217], v253 offset:32768
	ds_read_b64_tr_b16 v[218:219], v253 offset:36864
	v_cvt_pk_bf16_f32 v82, v81, v82
	v_cvt_pk_bf16_f32 v83, v83, v84
	v_cvt_pk_bf16_f32 v84, v85, v86
	v_cvt_pk_bf16_f32 v85, v87, v89
	s_nop 1
	s_waitcnt lgkmcnt(14)
	v_mfma_f32_16x16x32_bf16 v[86:89], v[188:191], v[82:85], v[2:5]
	s_waitcnt lgkmcnt(12)
	v_mfma_f32_16x16x32_bf16 v[58:61], v[192:195], v[82:85], v[58:61]
	s_ashr_i32 s43, s42, 31
	s_waitcnt lgkmcnt(10)
	v_mfma_f32_16x16x32_bf16 v[6:9], v[196:199], v[82:85], v[6:9]
	s_waitcnt lgkmcnt(8)
	v_mfma_f32_16x16x32_bf16 v[66:69], v[200:203], v[82:85], v[66:69]
	s_lshl_b64 s[16:17], s[42:43], 11
	s_waitcnt lgkmcnt(6)
	v_mfma_f32_16x16x32_bf16 v[62:65], v[204:207], v[82:85], v[62:65]
	s_waitcnt lgkmcnt(4)
	v_mfma_f32_16x16x32_bf16 v[70:73], v[208:211], v[82:85], v[70:73]
	v_add_f32_e32 v4, v79, v80
	v_rcp_f32_e32 v5, v4
	s_waitcnt lgkmcnt(2)
	v_mfma_f32_16x16x32_bf16 v[74:77], v[212:215], v[82:85], v[74:77]
	v_lshl_add_u32 v10, s5, 7, v108
	v_mul_lo_u32 v2, v10, s30
	v_mul_f32_e32 v10, v5, v86
	v_mul_f32_e32 v79, v5, v87
	v_mul_f32_e32 v6, v5, v6
	v_mul_f32_e32 v7, v5, v7
	v_cvt_pk_fp8_f32 v80, v10, v79
	v_cvt_pk_fp8_f32 v81, v6, v7
	s_waitcnt lgkmcnt(0)
	v_mfma_f32_16x16x32_bf16 v[54:57], v[216:219], v[82:85], v[54:57]
	v_mul_f32_e32 v82, v5, v88
	v_mul_f32_e32 v83, v5, v89
	v_mul_f32_e32 v6, v5, v8
	v_mul_f32_e32 v7, v5, v9
	v_cvt_pk_fp8_f32 v80, v82, v83 op_sel:[0,0,1]
	v_cvt_pk_fp8_f32 v81, v6, v7 op_sel:[0,0,1]
	v_mul_f32_e32 v6, v5, v58
	v_mul_f32_e32 v7, v5, v59
	v_cvt_pk_fp8_f32 v82, v6, v7
	v_mul_f32_e32 v6, v5, v62
	v_mul_f32_e32 v7, v5, v63
	v_cvt_pk_fp8_f32 v83, v6, v7
	v_mul_f32_e32 v8, v5, v60
	v_mul_f32_e32 v9, v5, v61
	v_mul_f32_e32 v6, v5, v64
	v_mul_f32_e32 v7, v5, v65
	v_cvt_pk_fp8_f32 v82, v8, v9 op_sel:[0,0,1]
	v_cvt_pk_fp8_f32 v83, v6, v7 op_sel:[0,0,1]
	v_mul_f32_e32 v7, v5, v66
	v_mul_f32_e32 v8, v5, v67
	v_cvt_pk_fp8_f32 v6, v7, v8
	v_mul_f32_e32 v8, v5, v74
	v_mul_f32_e32 v58, v5, v75
	v_cvt_pk_fp8_f32 v7, v8, v58
	v_mul_f32_e32 v9, v5, v68
	v_mul_f32_e32 v10, v5, v69
	v_cvt_pk_fp8_f32 v6, v9, v10 op_sel:[0,0,1]
	v_mul_f32_e32 v8, v5, v76
	v_mul_f32_e32 v9, v5, v77
	v_cvt_pk_fp8_f32 v7, v8, v9 op_sel:[0,0,1]
	v_mul_f32_e32 v9, v5, v70
	v_mul_f32_e32 v10, v5, v71
	v_cvt_pk_fp8_f32 v8, v9, v10
	v_mul_f32_e32 v10, v5, v54
	v_mul_f32_e32 v54, v5, v55
	v_cvt_pk_fp8_f32 v9, v10, v54
	s_ashr_i32 s5, s4, 31
	s_lshl_b64 s[4:5], s[4:5], 14
	v_add_u32_e32 v2, s1, v2
	s_add_u32 s4, s4, s16
	v_mul_f32_e32 v58, v5, v72
	v_mul_f32_e32 v59, v5, v73
	v_mul_f32_e32 v10, v5, v56
	v_mul_f32_e32 v5, v5, v57
	v_ashrrev_i32_e32 v3, 31, v2
	s_addc_u32 s5, s5, s17
	v_cvt_pk_fp8_f32 v8, v58, v59 op_sel:[0,0,1]
	v_cvt_pk_fp8_f32 v9, v10, v5 op_sel:[0,0,1]
	v_lshl_add_u64 v[2:3], s[4:5], 0, v[2:3]
	v_lshlrev_b64 v[12:13], 10, v[2:3]
	s_lshl_b32 s30, s0, 7
	v_lshl_add_u64 v[12:13], s[34:35], 0, v[12:13]
	v_lshl_add_u64 v[12:13], v[12:13], 0, s[30:31]
	v_permlane16_swap_b32_e32 v80, v81
	v_permlane16_swap_b32_e32 v82, v83
	v_permlane16_swap_b32_e32 v6, v7
	v_permlane16_swap_b32_e32 v8, v9
	v_permlane32_swap_b32_e32 v80, v82
	v_permlane32_swap_b32_e32 v81, v83
	v_lshl_add_u64 v[12:13], v[12:13], 0, v[100:101]
	v_permlane32_swap_b32_e32 v6, v8
	v_permlane32_swap_b32_e32 v7, v9
	global_store_dwordx4 v[12:13], v[80:83], off
	global_store_dwordx4 v[12:13], v[6:9], off offset:64
	s_and_saveexec_b64 s[4:5], s[8:9]
	s_cbranch_execz .LBB0_354
	v_log_f32_e32 v4, v4
	v_lshlrev_b64 v[2:3], 5, v[2:3]
	s_mov_b32 s1, s31
	v_lshl_add_u64 v[2:3], s[40:41], 0, v[2:3]
	v_add_f32_e32 v4, v78, v4
	v_mul_f32_e32 v4, 0x3f317218, v4
	v_lshl_add_u64 v[2:3], s[0:1], 2, v[2:3]
	global_store_dword v[2:3], v4, off
	s_branch .LBB0_354

.LBB0_399:
	s_and_b64 s[16:17], s[52:53], exec
	s_cselect_b32 s16, s43, s86
	v_add_u32_e32 v10, s16, v157
	v_add_u32_e32 v252, v10, v149
	ds_read_b64_tr_b16 v[188:189], v252 offset:16384
	ds_read_b64_tr_b16 v[190:191], v252 offset:20480
	v_add_u32_e32 v253, v10, v150
	ds_read_b64_tr_b16 v[192:193], v253 offset:16384
	ds_read_b64_tr_b16 v[194:195], v253 offset:20480
	v_add_u32_e32 v252, v10, v151
	ds_read_b64_tr_b16 v[196:197], v252 offset:16384
	ds_read_b64_tr_b16 v[198:199], v252 offset:20480
	v_add_u32_e32 v253, v10, v152
	ds_read_b64_tr_b16 v[200:201], v253 offset:16384
	ds_read_b64_tr_b16 v[202:203], v253 offset:20480
	v_add_u32_e32 v252, v10, v153
	ds_read_b64_tr_b16 v[204:205], v252 offset:16384
	ds_read_b64_tr_b16 v[206:207], v252 offset:20480
	v_add_u32_e32 v253, v10, v154
	ds_read_b64_tr_b16 v[208:209], v253 offset:16384
	ds_read_b64_tr_b16 v[210:211], v253 offset:20480
	v_add_u32_e32 v252, v10, v155
	ds_read_b64_tr_b16 v[212:213], v252 offset:16384
	ds_read_b64_tr_b16 v[214:215], v252 offset:20480
	v_add_u32_e32 v253, v10, v156
	ds_read_b64_tr_b16 v[216:217], v253 offset:16384
	ds_read_b64_tr_b16 v[218:219], v253 offset:20480
	v_cvt_pk_bf16_f32 v164, v164, v165
	v_cvt_pk_bf16_f32 v165, v166, v167
	v_cvt_pk_bf16_f32 v166, v168, v169
	v_cvt_pk_bf16_f32 v167, v170, v171
	s_nop 1
	s_waitcnt lgkmcnt(14)
	v_mfma_f32_16x16x32_bf16 v[2:5], v[188:191], v[164:167], v[2:5]
	s_waitcnt lgkmcnt(12)
	v_mfma_f32_16x16x32_bf16 v[6:9], v[192:195], v[164:167], v[6:9]
	s_waitcnt lgkmcnt(10)
	v_mfma_f32_16x16x32_bf16 v[58:61], v[196:199], v[164:167], v[58:61]
	s_waitcnt lgkmcnt(8)
	v_mfma_f32_16x16x32_bf16 v[62:65], v[200:203], v[164:167], v[62:65]
	s_waitcnt lgkmcnt(6)
	v_mfma_f32_16x16x32_bf16 v[66:69], v[204:207], v[164:167], v[66:69]
	s_waitcnt lgkmcnt(4)
	v_mfma_f32_16x16x32_bf16 v[74:77], v[208:211], v[164:167], v[74:77]
	s_waitcnt lgkmcnt(2)
	v_mfma_f32_16x16x32_bf16 v[70:73], v[212:215], v[164:167], v[70:73]
	s_waitcnt lgkmcnt(0)
	v_mfma_f32_16x16x32_bf16 v[54:57], v[216:219], v[164:167], v[54:57]
	s_andn2_b64 vcc, exec, s[62:63]
	s_cbranch_vccz .LBB0_395
	s_branch .LBB0_396
